# phase-0 RMSNorm loop: gain chunks loaded once before the loop; ladder waits re-derived from the in-order VMEM queue (loads still waited, trailing stores not drained)
# speedup vs baseline: 1.0101x; 1.0020x over previous
; #define GAS __attribute__((address_space(1)))
; template <int MODE, bool W8 = false>
; __device__ __forceinline__ void norm_rows(const Ctx& C, const void* src, bf16* xdst, const unsigned char* YS8, const int* srow, const float* gate, const float* gain, bf16* XN, float* outf, unsigned char* XN8 = nullptr) {
;     ...
;     for (int m0 = C.gw; m0 < T; m0 += NR * C.NGW) {
;         f32x4 v[NR][8]; unsigned ya[NR][8], yb[NR][8]; float h0[NR], h1[NR];
; #pragma unroll
;         for (int q = 0; q < NR; ++q) { const int m = m0 + q * C.NGW;
;             if (MODE == 0) { const GAS f32x4* xr = (const GAS f32x4*)((const float*)src + (size_t)m * DM) + C.lane;
; #pragma unroll
;                 for (int j = 0; j < 8; ++j) v[q][j] = xr[64 * j]; }
;     ...
;             float ss = 0.f;
; #pragma unroll
;             for (int j = 0; j < 8; ++j) ss += (v[q][j].x * v[q][j].x + v[q][j].y * v[q][j].y) + (v[q][j].z * v[q][j].z + v[q][j].w * v[q][j].w);
.LBB0_120:
	s_or_b64 exec, exec, s[12:13]
	s_cmpk_gt_i32 s16, 0x3fff
	s_cbranch_scc1 .LBB0_123
	v_mbcnt_lo_u32_b32 v2, -1, 0
	s_load_dwordx2 s[2:3], s[20:21], 0x10
	v_mbcnt_hi_u32_b32 v2, -1, v2
	v_and_b32_e32 v3, 64, v2
	v_add_u32_e32 v3, 64, v3
	v_xor_b32_e32 v4, 1, v2
	v_ashrrev_i32_e32 v1, 31, v0
	v_cmp_lt_i32_e32 vcc, v4, v3
	s_waitcnt vmcnt(24)
	v_lshlrev_b64 v[56:57], 4, v[0:1]
	s_waitcnt vmcnt(22) lgkmcnt(0)
	v_lshl_add_u64 v[58:59], s[2:3], 0, v[56:57]
	v_cndmask_b32_e32 v4, v2, v4, vcc
	s_waitcnt vmcnt(8)
	v_lshlrev_b32_e32 v73, 2, v4
	v_xor_b32_e32 v4, 2, v2
	s_mov_b64 s[2:3], 0x1000
	v_cmp_lt_i32_e32 vcc, v4, v3
	v_lshl_add_u64 v[60:61], v[58:59], 0, s[2:3]
	s_mov_b64 s[2:3], 0x1400
	v_cndmask_b32_e32 v4, v2, v4, vcc
	v_lshl_add_u64 v[62:63], v[58:59], 0, s[2:3]
	s_mov_b64 s[2:3], 0x1800
	s_waitcnt vmcnt(7)
	v_lshlrev_b32_e32 v74, 2, v4
	v_xor_b32_e32 v4, 4, v2
	v_lshl_add_u64 v[64:65], v[58:59], 0, s[2:3]
	s_mov_b64 s[2:3], 0x1c00
	v_cmp_lt_i32_e32 vcc, v4, v3
	v_lshl_add_u64 v[66:67], v[58:59], 0, s[2:3]
	s_add_i32 s2, s16, 0x800
	v_cndmask_b32_e32 v4, v2, v4, vcc
	s_ashr_i32 s3, s2, 31
	s_waitcnt vmcnt(6)
	v_lshlrev_b32_e32 v75, 2, v4
	v_xor_b32_e32 v4, 8, v2
	s_add_i32 s12, s16, 0xfffff000
	s_lshl_b64 s[4:5], s[2:3], 12
	v_cmp_lt_i32_e32 vcc, v4, v3
	s_add_u32 s4, s18, s4
	s_addc_u32 s5, s19, s5
	v_cndmask_b32_e32 v4, v2, v4, vcc
	s_lshl_b64 s[2:3], s[2:3], 13
	s_waitcnt vmcnt(5)
	v_lshlrev_b32_e32 v76, 2, v4
	v_xor_b32_e32 v4, 16, v2
	s_add_u32 s6, s8, s2
	v_cmp_lt_i32_e32 vcc, v4, v3
	s_addc_u32 s7, s9, s3
	s_ashr_i32 s17, s16, 31
	v_cndmask_b32_e32 v4, v2, v4, vcc
	s_lshl_b64 s[2:3], s[16:17], 13
	s_waitcnt vmcnt(4)
	v_lshlrev_b32_e32 v77, 2, v4
	v_xor_b32_e32 v4, 32, v2
	s_add_u32 s8, s8, s2
	v_cmp_lt_i32_e32 vcc, v4, v3
	s_addc_u32 s9, s9, s3
	s_lshl_b64 s[2:3], s[16:17], 12
	v_cndmask_b32_e32 v2, v2, v4, vcc
	s_add_u32 s10, s18, s2
	v_lshlrev_b32_e32 v78, 2, v2
	v_lshlrev_b64 v[68:69], 3, v[0:1]
	s_addc_u32 s11, s19, s3
	s_movk_i32 s13, 0x1000
	v_mov_b32_e32 v79, 0x358637bd
	s_mov_b32 s14, 0xf800000
	v_mov_b32_e32 v80, 0x260
	s_brev_b32 s15, 44
	global_load_dwordx4 v[160:163], v[58:59], off
	global_load_dwordx4 v[164:167], v[58:59], off offset:1024
	global_load_dwordx4 v[168:171], v[58:59], off offset:2048
	global_load_dwordx4 v[172:175], v[58:59], off offset:3072
	global_load_dwordx4 v[176:179], v[60:61], off
	global_load_dwordx4 v[180:183], v[62:63], off
	global_load_dwordx4 v[184:187], v[64:65], off
	global_load_dwordx4 v[188:191], v[66:67], off
	s_waitcnt vmcnt(0)
.LBB0_122:
	v_lshl_add_u64 v[16:17], s[8:9], 0, v[56:57]
	global_load_dwordx4 v[86:89], v[16:17], off
	global_load_dwordx4 v[90:93], v[16:17], off offset:1024
	global_load_dwordx4 v[52:55], v[16:17], off offset:2048
	global_load_dwordx4 v[44:47], v[16:17], off offset:3072
	v_add_co_u32_e32 v16, vcc, 0x1000, v16
	v_lshl_add_u64 v[18:19], s[6:7], 0, v[56:57]
	s_nop 0
	v_addc_co_u32_e32 v17, vcc, 0, v17, vcc
	global_load_dwordx4 v[12:15], v[18:19], off
	global_load_dwordx4 v[8:11], v[18:19], off offset:1024
	global_load_dwordx4 v[4:7], v[18:19], off offset:2048
	global_load_dwordx4 v[0:3], v[18:19], off offset:3072
	global_load_dwordx4 v[40:43], v[16:17], off offset:1024
	global_load_dwordx4 v[48:51], v[16:17], off
	global_load_dwordx4 v[32:35], v[16:17], off offset:3072
	global_load_dwordx4 v[36:39], v[16:17], off offset:2048
	v_lshl_add_u64 v[20:21], s[10:11], 0, v[68:69]
	v_add_co_u32_e32 v94, vcc, s13, v18
	v_add_co_u32_e64 v70, s[2:3], s15, v20
	s_nop 0
	v_addc_co_u32_e32 v95, vcc, 0, v19, vcc
	v_addc_co_u32_e64 v71, s[2:3], 0, v21, s[2:3]
	global_load_dwordx4 v[24:27], v[94:95], off
	global_load_dwordx4 v[20:23], v[94:95], off offset:1024
	global_load_dwordx4 v[28:31], v[94:95], off offset:2048
	global_load_dwordx4 v[16:19], v[94:95], off offset:3072
	s_addk_i32 s12, 0x1000
	s_waitcnt vmcnt(15)
	v_mov_b32_e32 v96, v87
	s_waitcnt vmcnt(14)
	v_mov_b32_e32 v97, v91
	v_mov_b32_e32 v100, v89
	v_mov_b32_e32 v101, v93
	v_mov_b32_e32 v94, v86
	v_mov_b32_e32 v95, v90
	v_mov_b32_e32 v98, v88
	v_mov_b32_e32 v99, v92
	s_waitcnt vmcnt(13)
	v_pk_mul_f32 v[102:103], v[54:55], v[54:55]
	v_pk_mul_f32 v[104:105], v[52:53], v[52:53]
	v_pk_mul_f32 v[96:97], v[96:97], v[96:97]
	v_pk_mul_f32 v[100:101], v[100:101], v[100:101]
	v_pk_mov_b32 v[108:109], v[104:105], v[102:103] op_sel:[1,0]
	v_mov_b32_e32 v105, v103
	v_pk_fma_f32 v[94:95], v[94:95], v[94:95], v[96:97]
	v_pk_fma_f32 v[96:97], v[98:99], v[98:99], v[100:101]
	s_waitcnt vmcnt(12)
	v_mul_f32_e32 v72, v45, v45
	v_mul_f32_e32 v106, v47, v47
	v_pk_add_f32 v[98:99], v[108:109], v[104:105]
	v_pk_add_f32 v[94:95], v[94:95], v[96:97]
	v_pk_fma_f32 v[102:103], v[44:45], v[44:45], v[72:73] op_sel_hi:[1,1,0]
	v_pk_fma_f32 v[106:107], v[46:47], v[46:47], v[106:107] op_sel_hi:[1,1,0]
	s_waitcnt vmcnt(6)
	v_mul_f32_e32 v81, v48, v48
	v_mul_f32_e32 v110, v49, v49
	v_pk_add_f32 v[98:99], v[98:99], v[98:99] op_sel:[0,1] op_sel_hi:[1,0]
	v_pk_add_f32 v[94:95], v[94:95], v[94:95] op_sel:[0,1] op_sel_hi:[1,0]
	v_pk_mul_f32 v[100:101], v[42:43], v[42:43]
	v_pk_mul_f32 v[104:105], v[40:41], v[40:41]
	v_mul_f32_e32 v103, v50, v50
	v_mul_f32_e32 v107, v51, v51
	v_mov_b32_e32 v99, v110
	v_mov_b32_e32 v95, v81
	v_pk_mov_b32 v[96:97], v[104:105], v[100:101] op_sel:[1,0]
	v_mov_b32_e32 v105, v101
	v_pk_add_f32 v[102:103], v[102:103], v[106:107]
	v_pk_add_f32 v[94:95], v[94:95], v[98:99]
	s_waitcnt vmcnt(4)
; #define GAS __attribute__((address_space(1)))
; __device__ __forceinline__ unsigned pk2(float lo, float hi) { f32x2_m v = {lo, hi}; bf16x2_m b = __builtin_convertvector(v, bf16x2_m); return __builtin_bit_cast(unsigned, b); }
; template <int MODE, bool W8 = false>
; __device__ __forceinline__ void norm_rows(const Ctx& C, const void* src, bf16* xdst, const unsigned char* YS8, const int* srow, const float* gate, const float* gain, bf16* XN, float* outf, unsigned char* XN8 = nullptr) {
;     ...
;             float ss = 0.f;
; #pragma unroll
;             for (int j = 0; j < 8; ++j) ss += (v[q][j].x * v[q][j].x + v[q][j].y * v[q][j].y) + (v[q][j].z * v[q][j].z + v[q][j].w * v[q][j].w);
;             const float rstd = 1.0f / sqrtf(wave_sum(ss) * (1.0f / DM) + RMS_EPS);
;             if (MODE == 1) { GAS v2u* xo = (GAS v2u*)(xdst + (size_t)m * DM) + C.lane;
; #pragma unroll
;                 for (int j = 0; j < 8; ++j) { v2u w; w.x = pk2(v[q][j].x, v[q][j].y); w.y = pk2(v[q][j].z, v[q][j].w); xo[64 * j] = w; } }
;             const GAS f32x4* gg = (const GAS f32x4*)gain + C.lane;
;             if (MODE <= 1) { GAS v2u* o = (GAS v2u*)(XN + (size_t)m * DM) + C.lane;
; #pragma unroll
;                 for (int j = 0; j < 8; ++j) { const f32x4 g = gg[64 * j]; const f32x4 y = v[q][j] * rstd * g; v2u w; w.x = pk2(y.x, y.y); w.y = pk2(y.z, y.w); o[64 * j] = w;
	v_mul_f32_e32 v72, v37, v37
	v_mul_f32_e32 v108, v39, v39
	v_pk_add_f32 v[96:97], v[96:97], v[104:105]
	v_pk_add_f32 v[94:95], v[94:95], v[102:103]
	v_mul_f32_e32 v111, v34, v34
	v_mul_f32_e32 v112, v35, v35
	v_mul_f32_e32 v113, v32, v32
	v_mul_f32_e32 v114, v33, v33
	v_pk_fma_f32 v[100:101], v[36:37], v[36:37], v[72:73] op_sel_hi:[1,1,0]
	v_pk_fma_f32 v[108:109], v[38:39], v[38:39], v[108:109] op_sel_hi:[1,1,0]
	v_pk_add_f32 v[96:97], v[96:97], v[96:97] op_sel:[0,1] op_sel_hi:[1,0]
	v_pk_add_f32 v[94:95], v[94:95], v[94:95] op_sel:[0,1] op_sel_hi:[1,0]
	v_mov_b32_e32 v101, v111
	v_mov_b32_e32 v109, v112
	v_mov_b32_e32 v97, v114
	v_mov_b32_e32 v95, v113
	v_pk_add_f32 v[100:101], v[100:101], v[108:109]
	v_pk_add_f32 v[94:95], v[94:95], v[96:97]
	s_nop 0
	v_pk_add_f32 v[94:95], v[94:95], v[100:101]
	s_nop 0
	v_add_f32_e32 v72, v94, v95
	ds_bpermute_b32 v81, v73, v72
	s_waitcnt lgkmcnt(0)
	v_add_f32_e32 v72, v72, v81
	ds_bpermute_b32 v81, v74, v72
	s_waitcnt lgkmcnt(0)
	v_add_f32_e32 v72, v72, v81
	ds_bpermute_b32 v81, v75, v72
	s_waitcnt lgkmcnt(0)
	v_add_f32_e32 v72, v72, v81
	ds_bpermute_b32 v81, v76, v72
	s_waitcnt lgkmcnt(0)
	v_add_f32_e32 v72, v72, v81
	ds_bpermute_b32 v81, v77, v72
	s_waitcnt lgkmcnt(0)
	v_add_f32_e32 v72, v72, v81
	ds_bpermute_b32 v81, v78, v72
	s_waitcnt lgkmcnt(0)
	v_add_f32_e32 v72, v72, v81
	v_fmamk_f32 v72, v72, 0x3a000000, v79
	v_mul_f32_e32 v81, 0x4f800000, v72
	v_cmp_gt_f32_e32 vcc, s14, v72
	s_nop 1
	v_cndmask_b32_e32 v72, v72, v81, vcc
	v_sqrt_f32_e32 v81, v72
	s_nop 0
	v_add_u32_e32 v94, -1, v81
	v_add_u32_e32 v95, 1, v81
	v_fma_f32 v96, -v94, v81, v72
	v_fma_f32 v97, -v95, v81, v72
	v_cmp_ge_f32_e64 s[2:3], 0, v96
	s_nop 1
	v_cndmask_b32_e64 v81, v81, v94, s[2:3]
	v_cmp_lt_f32_e64 s[2:3], 0, v97
	s_nop 1
	v_cndmask_b32_e64 v81, v81, v95, s[2:3]
	v_mul_f32_e32 v94, 0x37800000, v81
	v_cndmask_b32_e32 v81, v81, v94, vcc
	v_cmp_class_f32_e32 vcc, v72, v80
	s_nop 1
	v_cndmask_b32_e32 v72, v81, v72, vcc
	v_div_scale_f32 v81, s[2:3], v72, v72, 1.0
	v_rcp_f32_e32 v95, v81
	v_div_scale_f32 v94, vcc, 1.0, v72, 1.0
	v_fma_f32 v96, -v81, v95, 1.0
	v_fmac_f32_e32 v95, v96, v95
	v_mul_f32_e32 v96, v94, v95
	v_fma_f32 v97, -v81, v96, v94
	v_fmac_f32_e32 v96, v97, v95
	v_fma_f32 v81, -v81, v96, v94
	v_div_fmas_f32 v81, v81, v95, v96
	v_div_fixup_f32 v72, v81, v72, 1.0
	v_pk_mul_f32 v[86:87], v[86:87], v[72:73] op_sel_hi:[1,0]
	v_pk_mul_f32 v[88:89], v[88:89], v[72:73] op_sel_hi:[1,0]
	v_pk_mul_f32 v[82:83], v[160:161], v[86:87]
	v_pk_mul_f32 v[84:85], v[162:163], v[88:89]
	v_cvt_pk_bf16_f32 v82, v82, v83
	v_cvt_pk_bf16_f32 v83, v84, v85
	global_store_dwordx2 v[70:71], v[82:83], off
	s_nop 1
	v_pk_mul_f32 v[86:87], v[90:91], v[72:73] op_sel_hi:[1,0]
	v_pk_mul_f32 v[88:89], v[92:93], v[72:73] op_sel_hi:[1,0]
	v_pk_mul_f32 v[52:53], v[52:53], v[72:73] op_sel_hi:[1,0]
	v_pk_mul_f32 v[54:55], v[54:55], v[72:73] op_sel_hi:[1,0]
	v_pk_mul_f32 v[44:45], v[44:45], v[72:73] op_sel_hi:[1,0]
	v_pk_mul_f32 v[46:47], v[46:47], v[72:73] op_sel_hi:[1,0]
	v_pk_mul_f32 v[48:49], v[48:49], v[72:73] op_sel_hi:[1,0]
	v_pk_mul_f32 v[50:51], v[50:51], v[72:73] op_sel_hi:[1,0]
	v_pk_mul_f32 v[40:41], v[40:41], v[72:73] op_sel_hi:[1,0]
	v_pk_mul_f32 v[42:43], v[42:43], v[72:73] op_sel_hi:[1,0]
	v_pk_mul_f32 v[36:37], v[36:37], v[72:73] op_sel_hi:[1,0]
	v_pk_mul_f32 v[38:39], v[38:39], v[72:73] op_sel_hi:[1,0]
	v_pk_mul_f32 v[32:33], v[32:33], v[72:73] op_sel_hi:[1,0]
	v_pk_mul_f32 v[34:35], v[34:35], v[72:73] op_sel_hi:[1,0]
	s_waitcnt vmcnt(4)
	v_mul_f32_e32 v81, v24, v24
	s_waitcnt vmcnt(1)
	v_pk_mul_f32 v[84:85], v[166:167], v[88:89]
	v_pk_mul_f32 v[82:83], v[164:165], v[86:87]
	v_mul_f32_e32 v86, v16, v16
	v_cvt_pk_bf16_f32 v82, v82, v83
	v_cvt_pk_bf16_f32 v83, v84, v85
	global_store_dwordx2 v[70:71], v[82:83], off offset:512
	s_nop 1
	v_mul_f32_e32 v87, v17, v17
	v_mul_f32_e32 v88, v18, v18
	v_mul_f32_e32 v89, v19, v19
	v_pk_mul_f32 v[54:55], v[170:171], v[54:55]
	v_pk_mul_f32 v[52:53], v[168:169], v[52:53]
	v_pk_mul_f32 v[82:83], v[4:5], v[4:5]
	v_cvt_pk_bf16_f32 v52, v52, v53
	v_cvt_pk_bf16_f32 v53, v54, v55
	global_store_dwordx2 v[70:71], v[52:53], off offset:1024
	s_nop 1
	v_mul_f32_e32 v84, v1, v1
	v_pk_mul_f32 v[46:47], v[174:175], v[46:47]
	v_pk_mul_f32 v[44:45], v[172:173], v[44:45]
	v_mov_b32_e32 v52, v15
	v_cvt_pk_bf16_f32 v44, v44, v45
	v_cvt_pk_bf16_f32 v45, v46, v47
	global_store_dwordx2 v[70:71], v[44:45], off offset:1536
	s_nop 1
	v_mov_b32_e32 v53, v11
	v_pk_mul_f32 v[54:55], v[6:7], v[6:7]
	v_pk_mul_f32 v[46:47], v[178:179], v[50:51]
	v_pk_mul_f32 v[44:45], v[176:177], v[48:49]
	v_mov_b32_e32 v48, v13
	v_cvt_pk_bf16_f32 v44, v44, v45
	v_cvt_pk_bf16_f32 v45, v46, v47
	global_store_dwordx2 v[70:71], v[44:45], off offset:2048
	s_nop 1
	v_mov_b32_e32 v49, v9
	v_mov_b32_e32 v50, v14
	v_mov_b32_e32 v51, v10
	v_pk_mul_f32 v[42:43], v[42:43], v[182:183]
	v_pk_mul_f32 v[40:41], v[40:41], v[180:181]
	v_mov_b32_e32 v46, v12
	v_cvt_pk_bf16_f32 v40, v40, v41
	v_cvt_pk_bf16_f32 v41, v42, v43
	global_store_dwordx2 v[70:71], v[40:41], off offset:2560
	s_nop 1
	v_mov_b32_e32 v47, v8
	v_lshl_add_u64 v[44:45], s[4:5], 0, v[68:69]
	v_add_co_u32_e32 v44, vcc, s15, v44
	s_add_u32 s4, s4, 0x1000000
	s_nop 0
	v_addc_co_u32_e32 v45, vcc, 0, v45, vcc
	s_addc_u32 s5, s5, 0
	s_add_u32 s6, s6, 0x2000000
	s_addc_u32 s7, s7, 0
	s_add_u32 s8, s8, 0x2000000
	s_addc_u32 s9, s9, 0
	s_add_u32 s10, s10, 0x1000000
	s_addc_u32 s11, s11, 0
	s_cmpk_lt_i32 s12, 0x3000
	v_pk_mul_f32 v[38:39], v[38:39], v[186:187]
	v_pk_mul_f32 v[36:37], v[36:37], v[184:185]
	v_pk_mul_f32 v[42:43], v[48:49], v[48:49]
	v_cvt_pk_bf16_f32 v36, v36, v37
	v_cvt_pk_bf16_f32 v37, v38, v39
; #define GAS __attribute__((address_space(1)))
; __device__ __forceinline__ unsigned pk2(float lo, float hi) { f32x2_m v = {lo, hi}; bf16x2_m b = __builtin_convertvector(v, bf16x2_m); return __builtin_bit_cast(unsigned, b); }
; template <int MODE, bool W8 = false>
; __device__ __forceinline__ void norm_rows(const Ctx& C, const void* src, bf16* xdst, const unsigned char* YS8, const int* srow, const float* gate, const float* gain, bf16* XN, float* outf, unsigned char* XN8 = nullptr) {
;     ...
;             float ss = 0.f;
; #pragma unroll
;             for (int j = 0; j < 8; ++j) ss += (v[q][j].x * v[q][j].x + v[q][j].y * v[q][j].y) + (v[q][j].z * v[q][j].z + v[q][j].w * v[q][j].w);
;             const float rstd = 1.0f / sqrtf(wave_sum(ss) * (1.0f / DM) + RMS_EPS);
;             if (MODE == 1) { GAS v2u* xo = (GAS v2u*)(xdst + (size_t)m * DM) + C.lane;
; #pragma unroll
;                 for (int j = 0; j < 8; ++j) { v2u w; w.x = pk2(v[q][j].x, v[q][j].y); w.y = pk2(v[q][j].z, v[q][j].w); xo[64 * j] = w; } }
;             const GAS f32x4* gg = (const GAS f32x4*)gain + C.lane;
;             if (MODE <= 1) { GAS v2u* o = (GAS v2u*)(XN + (size_t)m * DM) + C.lane;
; #pragma unroll
;                 for (int j = 0; j < 8; ++j) { const f32x4 g = gg[64 * j]; const f32x4 y = v[q][j] * rstd * g; v2u w; w.x = pk2(y.x, y.y); w.y = pk2(y.z, y.w); o[64 * j] = w;
	global_store_dwordx2 v[70:71], v[36:37], off offset:3072
	s_nop 1
	v_pk_mul_f32 v[48:49], v[52:53], v[52:53]
	v_mul_f32_e32 v40, v3, v3
	v_pk_mov_b32 v[52:53], v[82:83], v[54:55] op_sel:[1,0]
	v_mov_b32_e32 v83, v55
	v_pk_fma_f32 v[42:43], v[46:47], v[46:47], v[42:43]
	v_pk_fma_f32 v[46:47], v[50:51], v[50:51], v[48:49]
	v_pk_fma_f32 v[40:41], v[2:3], v[2:3], v[40:41] op_sel_hi:[1,1,0]
	v_pk_add_f32 v[48:49], v[52:53], v[82:83]
	v_pk_add_f32 v[42:43], v[42:43], v[46:47]
	v_pk_fma_f32 v[54:55], v[0:1], v[0:1], v[84:85] op_sel_hi:[1,1,0]
	v_mul_f32_e32 v41, v25, v25
	v_mul_f32_e32 v83, v27, v27
	v_pk_add_f32 v[46:47], v[48:49], v[48:49] op_sel:[0,1] op_sel_hi:[1,0]
	v_pk_add_f32 v[42:43], v[42:43], v[42:43] op_sel:[0,1] op_sel_hi:[1,0]
	v_mul_f32_e32 v55, v26, v26
	v_pk_mul_f32 v[48:49], v[22:23], v[22:23]
	v_pk_mul_f32 v[50:51], v[20:21], v[20:21]
	v_mov_b32_e32 v47, v41
	v_mov_b32_e32 v41, v83
	v_mov_b32_e32 v43, v81
	v_pk_mov_b32 v[84:85], v[50:51], v[48:49] op_sel:[1,0]
	v_mov_b32_e32 v51, v49
	v_pk_add_f32 v[40:41], v[54:55], v[40:41]
	v_pk_add_f32 v[42:43], v[42:43], v[46:47]
	v_mul_f32_e32 v52, v29, v29
	v_mul_f32_e32 v82, v31, v31
	v_pk_add_f32 v[50:51], v[84:85], v[50:51]
	v_pk_add_f32 v[40:41], v[42:43], v[40:41]
	v_pk_fma_f32 v[48:49], v[28:29], v[28:29], v[52:53] op_sel_hi:[1,1,0]
	v_pk_fma_f32 v[52:53], v[30:31], v[30:31], v[82:83] op_sel_hi:[1,1,0]
	v_pk_add_f32 v[46:47], v[50:51], v[50:51] op_sel:[0,1] op_sel_hi:[1,0]
	v_pk_add_f32 v[40:41], v[40:41], v[40:41] op_sel:[0,1] op_sel_hi:[1,0]
	v_mov_b32_e32 v49, v88
	v_mov_b32_e32 v53, v89
	v_mov_b32_e32 v47, v87
	v_mov_b32_e32 v41, v86
	v_pk_add_f32 v[48:49], v[48:49], v[52:53]
	v_pk_add_f32 v[40:41], v[40:41], v[46:47]
	v_pk_mul_f32 v[34:35], v[34:35], v[190:191]
	v_pk_mul_f32 v[32:33], v[32:33], v[188:189]
	v_pk_add_f32 v[40:41], v[40:41], v[48:49]
	v_cvt_pk_bf16_f32 v32, v32, v33
	v_cvt_pk_bf16_f32 v33, v34, v35
	global_store_dwordx2 v[70:71], v[32:33], off offset:3584
	s_nop 1
	v_add_f32_e32 v40, v40, v41
	ds_bpermute_b32 v41, v73, v40
	s_waitcnt lgkmcnt(0)
	v_add_f32_e32 v40, v40, v41
	ds_bpermute_b32 v41, v74, v40
	s_waitcnt lgkmcnt(0)
	v_add_f32_e32 v40, v40, v41
	ds_bpermute_b32 v36, v75, v40
	s_waitcnt lgkmcnt(0)
	v_add_f32_e32 v36, v40, v36
	ds_bpermute_b32 v37, v76, v36
	s_waitcnt lgkmcnt(0)
	v_add_f32_e32 v36, v36, v37
	ds_bpermute_b32 v37, v77, v36
	s_waitcnt lgkmcnt(0)
	v_add_f32_e32 v36, v36, v37
	ds_bpermute_b32 v37, v78, v36
	s_waitcnt lgkmcnt(0)
	v_add_f32_e32 v36, v36, v37
	v_fmamk_f32 v36, v36, 0x3a000000, v79
	v_mul_f32_e32 v37, 0x4f800000, v36
	v_cmp_gt_f32_e32 vcc, s14, v36
	s_nop 1
	v_cndmask_b32_e32 v36, v36, v37, vcc
	v_sqrt_f32_e32 v37, v36
	s_nop 0
	v_add_u32_e32 v38, -1, v37
	v_add_u32_e32 v39, 1, v37
	v_fma_f32 v40, -v38, v37, v36
	v_fma_f32 v41, -v39, v37, v36
	v_cmp_ge_f32_e64 s[2:3], 0, v40
	s_nop 1
	v_cndmask_b32_e64 v37, v37, v38, s[2:3]
	v_cmp_lt_f32_e64 s[2:3], 0, v41
	s_nop 1
	v_cndmask_b32_e64 v37, v37, v39, s[2:3]
	v_mul_f32_e32 v38, 0x37800000, v37
	v_cndmask_b32_e32 v37, v37, v38, vcc
	v_cmp_class_f32_e32 vcc, v36, v80
	s_nop 1
	v_cndmask_b32_e32 v36, v37, v36, vcc
	v_div_scale_f32 v37, s[2:3], v36, v36, 1.0
	v_rcp_f32_e32 v39, v37
	v_div_scale_f32 v38, vcc, 1.0, v36, 1.0
	v_fma_f32 v40, -v37, v39, 1.0
	v_fmac_f32_e32 v39, v40, v39
	v_mul_f32_e32 v40, v38, v39
	v_fma_f32 v41, -v37, v40, v38
	v_fmac_f32_e32 v40, v41, v39
	v_fma_f32 v37, -v37, v40, v38
	v_div_fmas_f32 v37, v37, v39, v40
	v_div_fixup_f32 v36, v37, v36, 1.0
	v_pk_mul_f32 v[12:13], v[12:13], v[36:37] op_sel_hi:[1,0]
	v_pk_mul_f32 v[14:15], v[14:15], v[36:37] op_sel_hi:[1,0]
	v_pk_mul_f32 v[12:13], v[160:161], v[12:13]
	v_pk_mul_f32 v[14:15], v[162:163], v[14:15]
	v_cvt_pk_bf16_f32 v12, v12, v13
	v_cvt_pk_bf16_f32 v13, v14, v15
	global_store_dwordx2 v[44:45], v[12:13], off
	s_nop 1
	v_pk_mul_f32 v[8:9], v[8:9], v[36:37] op_sel_hi:[1,0]
	v_pk_mul_f32 v[10:11], v[10:11], v[36:37] op_sel_hi:[1,0]
	v_pk_mul_f32 v[4:5], v[4:5], v[36:37] op_sel_hi:[1,0]
	v_pk_mul_f32 v[6:7], v[6:7], v[36:37] op_sel_hi:[1,0]
	v_pk_mul_f32 v[0:1], v[0:1], v[36:37] op_sel_hi:[1,0]
	v_pk_mul_f32 v[2:3], v[2:3], v[36:37] op_sel_hi:[1,0]
	v_pk_mul_f32 v[10:11], v[166:167], v[10:11]
	v_pk_mul_f32 v[8:9], v[164:165], v[8:9]
	s_nop 0
	v_cvt_pk_bf16_f32 v8, v8, v9
	v_cvt_pk_bf16_f32 v9, v10, v11
	global_store_dwordx2 v[44:45], v[8:9], off offset:512
	s_nop 1
	v_pk_mul_f32 v[6:7], v[170:171], v[6:7]
	v_pk_mul_f32 v[4:5], v[168:169], v[4:5]
	s_nop 0
	v_cvt_pk_bf16_f32 v4, v4, v5
	v_cvt_pk_bf16_f32 v5, v6, v7
	global_store_dwordx2 v[44:45], v[4:5], off offset:1024
	s_nop 1
	v_pk_mul_f32 v[2:3], v[174:175], v[2:3]
	v_pk_mul_f32 v[0:1], v[172:173], v[0:1]
	v_pk_mul_f32 v[4:5], v[24:25], v[36:37] op_sel_hi:[1,0]
	v_cvt_pk_bf16_f32 v0, v0, v1
	v_cvt_pk_bf16_f32 v1, v2, v3
	global_store_dwordx2 v[44:45], v[0:1], off offset:1536
	s_nop 1
	v_pk_mul_f32 v[6:7], v[26:27], v[36:37] op_sel_hi:[1,0]
	v_pk_mul_f32 v[0:1], v[176:177], v[4:5]
	v_pk_mul_f32 v[2:3], v[178:179], v[6:7]
	v_cvt_pk_bf16_f32 v0, v0, v1
	v_cvt_pk_bf16_f32 v1, v2, v3
	global_store_dwordx2 v[44:45], v[0:1], off offset:2048
	s_nop 1
	v_pk_mul_f32 v[4:5], v[20:21], v[36:37] op_sel_hi:[1,0]
	v_pk_mul_f32 v[6:7], v[22:23], v[36:37] op_sel_hi:[1,0]
	v_pk_mul_f32 v[0:1], v[4:5], v[180:181]
	v_pk_mul_f32 v[2:3], v[6:7], v[182:183]
	v_cvt_pk_bf16_f32 v0, v0, v1
	v_cvt_pk_bf16_f32 v1, v2, v3
	global_store_dwordx2 v[44:45], v[0:1], off offset:2560
	s_nop 1
	v_pk_mul_f32 v[4:5], v[28:29], v[36:37] op_sel_hi:[1,0]
	v_pk_mul_f32 v[6:7], v[30:31], v[36:37] op_sel_hi:[1,0]
	v_pk_mul_f32 v[0:1], v[4:5], v[184:185]
	v_pk_mul_f32 v[2:3], v[6:7], v[186:187]
	v_cvt_pk_bf16_f32 v0, v0, v1
	v_cvt_pk_bf16_f32 v1, v2, v3
	global_store_dwordx2 v[44:45], v[0:1], off offset:3072
	s_nop 1
	v_pk_mul_f32 v[4:5], v[16:17], v[36:37] op_sel_hi:[1,0]
	v_pk_mul_f32 v[6:7], v[18:19], v[36:37] op_sel_hi:[1,0]
	v_pk_mul_f32 v[0:1], v[4:5], v[188:189]
	v_pk_mul_f32 v[2:3], v[6:7], v[190:191]
	v_cvt_pk_bf16_f32 v0, v0, v1
	v_cvt_pk_bf16_f32 v1, v2, v3
	global_store_dwordx2 v[44:45], v[0:1], off offset:3584
	s_nop 1
	s_cbranch_scc1 .LBB0_122
